# speedup vs baseline: 1.0026x; 1.0026x over previous
.LBB0_4:
	s_mov_b32 s12, -1
	s_mov_b32 s13, 0
	s_mov_b32 s14, 0xffff
	s_mov_b32 s15, 0xffff
	s_load_dwordx8 s[4:11], s[0:1], 0x20
	v_lshrrev_b32_e32 v1, 5, v0
	v_lshlrev_b32_e32 v0, 2, v0
	s_lshl_b32 s0, s2, 3
	v_and_b32_e32 v50, 0xfc, v0
	s_addk_i32 s0, 0xf280
	v_lshlrev_b32_e32 v24, 2, v50
	v_mov_b32_e32 v25, 0
	v_and_or_b32 v45, v1, 6, s0
	s_waitcnt lgkmcnt(0)
	v_lshl_add_u64 v[4:5], s[4:5], 0, v[24:25]
	s_movk_i32 s2, 0xc00
	v_mad_i64_i32 v[6:7], s[0:1], v45, s2, v[4:5]
	global_load_dwordx4 v[16:19], v[6:7], off nt
	global_load_dwordx4 v[20:23], v[6:7], off offset:1024 nt
	global_load_dwordx4 v[0:3], v[6:7], off offset:2048 nt
	v_mbcnt_lo_u32_b32 v6, -1, 0
	v_mbcnt_hi_u32_b32 v30, -1, v6
	v_and_b32_e32 v6, 64, v30
	v_mov_b32_e32 v8, v25
	v_xor_b32_e32 v7, 32, v30
	v_add_u32_e32 v33, 64, v6
	v_cmp_lt_i32_e32 vcc, v7, v33
	v_or_b32_e32 v52, 1, v45
	v_xor_b32_e32 v31, 16, v30
	v_cndmask_b32_e32 v6, v30, v7, vcc
	v_lshlrev_b32_e32 v53, 2, v6
	v_mad_i64_i32 v[10:11], s[0:1], v52, s2, v[4:5]
	v_xor_b32_e32 v32, 8, v30
	global_load_dwordx4 v[4:7], v[10:11], off nt
	v_cmp_lt_i32_e32 vcc, v31, v33
	v_mov_b32_e32 v59, 0x3727c5ac
	s_mov_b32 s2, 0xf800000
	v_mov_b32_e32 v60, 0x260
	s_movk_i32 s3, 0x600
	s_waitcnt vmcnt(3)
	v_mov_b32_e32 v12, v17
	v_mov_b32_e32 v13, v18
	v_mov_b32_e32 v14, v16
	v_mov_b32_e32 v15, v19
	v_pk_add_f32 v[12:13], v[12:13], v[14:15]
	s_waitcnt vmcnt(2)
	v_add_f32_e32 v26, v20, v21
	v_pk_add_f32 v[12:13], v[12:13], v[12:13] op_sel:[0,1] op_sel_hi:[1,0]
	v_add_f32_e32 v28, v22, v23
	s_waitcnt vmcnt(1)
	v_mov_b32_e32 v9, v1
	v_mov_b32_e32 v27, v2
	v_mov_b32_e32 v29, v3
	v_mov_b32_e32 v13, v0
	v_pk_add_f32 v[14:15], v[26:27], v[28:29]
	v_pk_add_f32 v[8:9], v[12:13], v[8:9]
	v_cndmask_b32_e32 v12, v30, v31, vcc
	v_pk_add_f32 v[8:9], v[8:9], v[14:15]
	v_cmp_lt_i32_e32 vcc, v32, v33
	v_add_f32_e32 v8, v8, v9
	v_mov_b32_e32 v9, v8
	v_mov_b32_e32 v62, v8
	s_nop 1
	v_permlane32_swap_b32_e32 v9, v62
	v_cndmask_b32_e64 v9, v9, v62, s[12:13]
	v_lshlrev_b32_e32 v54, 2, v12
	global_load_dwordx4 v[12:15], v[10:11], off offset:1024 nt
	v_xor_b32_e32 v28, 4, v30
	s_waitcnt lgkmcnt(0)
	v_add_f32_e32 v26, v8, v9
	v_cndmask_b32_e32 v8, v30, v32, vcc
	v_lshlrev_b32_e32 v55, 2, v8
	global_load_dwordx4 v[8:11], v[10:11], off offset:2048 nt
	v_mov_b32_e32 v27, v26
	v_mov_b32_e32 v62, v26
	s_nop 1
	v_permlane16_swap_b32_e32 v27, v62
	v_cndmask_b32_e64 v27, v27, v62, s[14:15]
	v_cmp_lt_i32_e32 vcc, v28, v33
	s_waitcnt lgkmcnt(0)
	v_add_f32_e32 v26, v26, v27
	s_nop 1
	v_mov_b32_dpp v27, v26 row_ror:8 row_mask:0xf bank_mask:0xf
	v_cndmask_b32_e32 v28, v30, v28, vcc
	v_lshlrev_b32_e32 v56, 2, v28
	v_xor_b32_e32 v28, 2, v30
	v_cmp_lt_i32_e32 vcc, v28, v33
	s_waitcnt lgkmcnt(0)
	v_add_f32_e32 v26, v26, v27
	s_nop 1
	v_mov_b32_dpp v27, v26 row_shl:4 row_mask:0xf bank_mask:0x5
	v_mov_b32_dpp v27, v26 row_shr:4 row_mask:0xf bank_mask:0xa
	v_cndmask_b32_e32 v28, v30, v28, vcc
	v_lshlrev_b32_e32 v57, 2, v28
	v_xor_b32_e32 v28, 1, v30
	v_cmp_lt_i32_e32 vcc, v28, v33
	s_waitcnt lgkmcnt(0)
	v_add_f32_e32 v26, v26, v27
	s_nop 1
	v_mov_b32_dpp v27, v26 quad_perm:[2,3,0,1] row_mask:0xf bank_mask:0xf
	v_cndmask_b32_e32 v28, v30, v28, vcc
	v_lshlrev_b32_e32 v58, 2, v28
	s_waitcnt lgkmcnt(0)
	v_add_f32_e32 v26, v26, v27
	s_nop 1
	v_mov_b32_dpp v27, v26 quad_perm:[1,0,3,2] row_mask:0xf bank_mask:0xf
	s_waitcnt lgkmcnt(0)
	v_add_f32_e32 v26, v26, v27
	v_fmamk_f32 v34, v26, 0xbaaaaaab, v16
	v_fmac_f32_e32 v18, 0xbaaaaaab, v26
	v_fmamk_f32 v36, v26, 0xbaaaaaab, v20
	v_fmac_f32_e32 v22, 0xbaaaaaab, v26
	v_fmamk_f32 v35, v26, 0xbaaaaaab, v17
	v_fmamk_f32 v19, v26, 0xbaaaaaab, v19
	v_fmamk_f32 v37, v26, 0xbaaaaaab, v21
	v_fmamk_f32 v23, v26, 0xbaaaaaab, v23
	v_fmamk_f32 v3, v26, 0xbaaaaaab, v3
	v_fmamk_f32 v2, v26, 0xbaaaaaab, v2
	v_fmamk_f32 v1, v26, 0xbaaaaaab, v1
	v_fmac_f32_e32 v0, 0xbaaaaaab, v26
	v_mul_f32_e32 v16, v34, v34
	v_mul_f32_e32 v20, v18, v18
	v_mul_f32_e32 v26, v36, v36
	v_mul_f32_e32 v28, v22, v22
	v_pk_fma_f32 v[16:17], v[34:35], v[34:35], v[16:17] op_sel_hi:[1,1,0]
	v_pk_fma_f32 v[20:21], v[18:19], v[18:19], v[20:21] op_sel_hi:[1,1,0]
	v_pk_fma_f32 v[26:27], v[36:37], v[36:37], v[26:27] op_sel_hi:[1,1,0]
	v_pk_fma_f32 v[28:29], v[22:23], v[22:23], v[28:29] op_sel_hi:[1,1,0]
	v_mul_f32_e32 v16, v0, v0
	v_mul_f32_e32 v20, v1, v1
	v_mul_f32_e32 v26, v2, v2
	v_mul_f32_e32 v28, v3, v3
	v_pk_add_f32 v[16:17], v[16:17], v[20:21]
	v_pk_add_f32 v[20:21], v[26:27], v[28:29]
	s_waitcnt vmcnt(2)
	v_mov_b32_e32 v26, v4
	v_pk_add_f32 v[16:17], v[16:17], v[20:21]
	v_mov_b32_e32 v20, v5
	v_add_f32_e32 v16, v16, v17
	v_mov_b32_e32 v17, v16
	v_mov_b32_e32 v62, v16
	s_nop 1
	v_permlane32_swap_b32_e32 v17, v62
	v_cndmask_b32_e64 v17, v17, v62, s[12:13]
	v_mov_b32_e32 v27, v7
	s_waitcnt lgkmcnt(0)
	v_add_f32_e32 v16, v16, v17
	v_mov_b32_e32 v17, v16
	v_mov_b32_e32 v62, v16
	s_nop 1
	v_permlane16_swap_b32_e32 v17, v62
	v_cndmask_b32_e64 v17, v17, v62, s[14:15]
	s_waitcnt lgkmcnt(0)
	v_add_f32_e32 v17, v16, v17
	s_nop 1
	v_mov_b32_dpp v21, v17 row_ror:8 row_mask:0xf bank_mask:0xf
	v_mov_b32_e32 v16, v25
	s_waitcnt vmcnt(1)
	v_add_f32_e32 v28, v12, v13
	v_add_f32_e32 v30, v14, v15
	s_waitcnt lgkmcnt(0)
	v_add_f32_e32 v17, v17, v21
	s_nop 1
	v_mov_b32_dpp v29, v17 row_shl:4 row_mask:0xf bank_mask:0x5
	v_mov_b32_dpp v29, v17 row_shr:4 row_mask:0xf bank_mask:0xa
	v_mov_b32_e32 v21, v6
	v_pk_add_f32 v[20:21], v[20:21], v[26:27]
	s_waitcnt vmcnt(0)
	v_mov_b32_e32 v31, v11
	v_pk_add_f32 v[20:21], v[20:21], v[20:21] op_sel:[0,1] op_sel_hi:[1,0]
	s_waitcnt lgkmcnt(0)
	v_add_f32_e32 v17, v17, v29
	s_nop 1
	v_mov_b32_dpp v32, v17 quad_perm:[2,3,0,1] row_mask:0xf bank_mask:0xf
	v_mov_b32_e32 v21, v8
	v_mov_b32_e32 v29, v10
	v_pk_add_f32 v[38:39], v[28:29], v[30:31]
	s_waitcnt lgkmcnt(0)
	v_add_f32_e32 v40, v17, v32
	s_nop 1
	v_mov_b32_dpp v41, v40 quad_perm:[1,0,3,2] row_mask:0xf bank_mask:0xf
	v_mov_b32_e32 v17, v9
	v_pk_add_f32 v[16:17], v[20:21], v[16:17]
	global_load_dwordx4 v[26:29], v24, s[6:7]
	global_load_dwordx4 v[30:33], v24, s[8:9]
	s_waitcnt lgkmcnt(0)
	v_add_f32_e32 v40, v40, v41
	v_fmamk_f32 v40, v40, 0x3aaaaaab, v59
	v_mul_f32_e32 v41, 0x4f800000, v40
	v_cmp_gt_f32_e32 vcc, s2, v40
	s_nop 1
	v_cndmask_b32_e32 v40, v40, v41, vcc
	v_sqrt_f32_e32 v41, v40
	s_nop 0
	v_add_u32_e32 v20, -1, v41
	v_add_u32_e32 v21, 1, v41
	v_fma_f32 v42, -v20, v41, v40
	v_cmp_ge_f32_e64 s[0:1], 0, v42
	v_fma_f32 v42, -v21, v41, v40
	s_nop 0
	v_cndmask_b32_e64 v20, v41, v20, s[0:1]
	v_cmp_lt_f32_e64 s[0:1], 0, v42
	v_pk_add_f32 v[42:43], v[16:17], v[38:39]
	s_nop 0
	v_cndmask_b32_e64 v20, v20, v21, s[0:1]
	v_mul_f32_e32 v21, 0x37800000, v20
	v_cndmask_b32_e32 v20, v20, v21, vcc
	v_cmp_class_f32_e32 vcc, v40, v60
	v_add_f32_e32 v42, v42, v43
	v_mov_b32_e32 v43, v42
	v_mov_b32_e32 v62, v42
	s_nop 1
	v_permlane32_swap_b32_e32 v43, v62
	v_cndmask_b32_e64 v43, v43, v62, s[12:13]
	v_cndmask_b32_e32 v20, v20, v40, vcc
	v_div_scale_f32 v21, s[0:1], v20, v20, 1.0
	v_rcp_f32_e32 v40, v21
	v_div_scale_f32 v16, vcc, 1.0, v20, 1.0
	s_waitcnt lgkmcnt(0)
	v_add_f32_e32 v42, v42, v43
	v_fma_f32 v17, -v21, v40, 1.0
	v_fmac_f32_e32 v40, v17, v40
	v_mul_f32_e32 v17, v16, v40
	v_fma_f32 v38, -v21, v17, v16
	v_fmac_f32_e32 v17, v38, v40
	v_fma_f32 v16, -v21, v17, v16
	v_div_fmas_f32 v16, v16, v40, v17
	v_div_fixup_f32 v44, v16, v20, 1.0
	v_pk_mul_f32 v[38:39], v[18:19], v[44:45] op_sel_hi:[1,0]
	v_pk_mul_f32 v[40:41], v[22:23], v[44:45] op_sel_hi:[1,0]
	global_load_dwordx4 v[16:19], v24, s[6:7] offset:1024
	global_load_dwordx4 v[20:23], v24, s[8:9] offset:1024
	v_mov_b32_e32 v43, v42
	v_mov_b32_e32 v62, v42
	s_nop 1
	v_permlane16_swap_b32_e32 v43, v62
	v_cndmask_b32_e64 v43, v43, v62, s[14:15]
	v_pk_mul_f32 v[34:35], v[34:35], v[44:45] op_sel_hi:[1,0]
	v_pk_mul_f32 v[36:37], v[36:37], v[44:45] op_sel_hi:[1,0]
	s_waitcnt lgkmcnt(0)
	v_add_f32_e32 v42, v42, v43
	s_nop 1
	v_mov_b32_dpp v43, v42 row_ror:8 row_mask:0xf bank_mask:0xf
	s_waitcnt lgkmcnt(0)
	v_add_f32_e32 v42, v42, v43
	s_nop 1
	v_mov_b32_dpp v43, v42 row_shl:4 row_mask:0xf bank_mask:0x5
	v_mov_b32_dpp v43, v42 row_shr:4 row_mask:0xf bank_mask:0xa
	s_waitcnt lgkmcnt(0)
	v_add_f32_e32 v42, v42, v43
	s_nop 1
	v_mov_b32_dpp v43, v42 quad_perm:[2,3,0,1] row_mask:0xf bank_mask:0xf
	s_waitcnt lgkmcnt(0)
	v_add_f32_e32 v42, v42, v43
	s_nop 1
	v_mov_b32_dpp v43, v42 quad_perm:[1,0,3,2] row_mask:0xf bank_mask:0xf
	s_waitcnt vmcnt(2)
	v_pk_fma_f32 v[38:39], v[28:29], v[38:39], v[32:33]
	v_pk_fma_f32 v[34:35], v[26:27], v[34:35], v[30:31]
	v_cvt_pk_f16_f32 v47, v38, v39
	v_cvt_pk_f16_f32 v46, v34, v35
	s_waitcnt vmcnt(0)
	v_pk_fma_f32 v[40:41], v[18:19], v[40:41], v[22:23]
	v_pk_fma_f32 v[36:37], v[16:17], v[36:37], v[20:21]
	v_cvt_pk_f16_f32 v49, v40, v41
	v_cvt_pk_f16_f32 v48, v36, v37
	global_load_dwordx4 v[34:37], v24, s[6:7] offset:2048
	global_load_dwordx4 v[38:41], v24, s[8:9] offset:2048
	v_lshlrev_b32_e32 v24, 1, v50
	v_lshl_add_u64 v[24:25], s[10:11], 0, v[24:25]
	v_mad_i64_i32 v[50:51], s[0:1], v45, s3, v[24:25]
	s_waitcnt lgkmcnt(0)
	v_add_f32_e32 v45, v42, v43
	v_fmamk_f32 v4, v45, 0xbaaaaaab, v4
	v_fmamk_f32 v5, v45, 0xbaaaaaab, v5
	v_mul_f32_e32 v42, v4, v4
	v_fmac_f32_e32 v6, 0xbaaaaaab, v45
	v_pk_fma_f32 v[42:43], v[4:5], v[4:5], v[42:43] op_sel_hi:[1,1,0]
	v_fmamk_f32 v7, v45, 0xbaaaaaab, v7
	v_mul_f32_e32 v42, v6, v6
	global_store_dwordx2 v[50:51], v[46:47], off
	v_pk_fma_f32 v[46:47], v[6:7], v[6:7], v[42:43] op_sel_hi:[1,1,0]
	v_fmamk_f32 v9, v45, 0xbaaaaaab, v9
	v_fmac_f32_e32 v8, 0xbaaaaaab, v45
	v_mul_f32_e32 v42, v8, v8
	v_mul_f32_e32 v46, v9, v9
	v_fmamk_f32 v12, v45, 0xbaaaaaab, v12
	v_pk_add_f32 v[42:43], v[42:43], v[46:47]
	v_fmamk_f32 v13, v45, 0xbaaaaaab, v13
	v_mul_f32_e32 v46, v12, v12
	v_fmac_f32_e32 v14, 0xbaaaaaab, v45
	v_pk_fma_f32 v[46:47], v[12:13], v[12:13], v[46:47] op_sel_hi:[1,1,0]
	v_fmamk_f32 v15, v45, 0xbaaaaaab, v15
	v_mul_f32_e32 v46, v14, v14
	global_store_dwordx2 v[50:51], v[48:49], off offset:512
	v_fmamk_f32 v11, v45, 0xbaaaaaab, v11
	v_fmamk_f32 v10, v45, 0xbaaaaaab, v10
	v_pk_fma_f32 v[48:49], v[14:15], v[14:15], v[46:47] op_sel_hi:[1,1,0]
	v_mul_f32_e32 v46, v10, v10
	v_mul_f32_e32 v48, v11, v11
	v_pk_add_f32 v[46:47], v[46:47], v[48:49]
	v_pk_mul_f32 v[0:1], v[0:1], v[44:45] op_sel_hi:[1,0]
	v_pk_add_f32 v[42:43], v[42:43], v[46:47]
	v_pk_mul_f32 v[2:3], v[2:3], v[44:45] op_sel_hi:[1,0]
	v_add_f32_e32 v42, v42, v43
	v_mov_b32_e32 v43, v42
	v_mov_b32_e32 v62, v42
	s_nop 1
	v_permlane32_swap_b32_e32 v43, v62
	v_cndmask_b32_e64 v43, v43, v62, s[12:13]
	s_waitcnt lgkmcnt(0)
	v_add_f32_e32 v42, v42, v43
	v_mov_b32_e32 v43, v42
	v_mov_b32_e32 v62, v42
	s_nop 1
	v_permlane16_swap_b32_e32 v43, v62
	v_cndmask_b32_e64 v43, v43, v62, s[14:15]
	s_waitcnt lgkmcnt(0)
	v_add_f32_e32 v42, v42, v43
	s_nop 1
	v_mov_b32_dpp v43, v42 row_ror:8 row_mask:0xf bank_mask:0xf
	s_waitcnt lgkmcnt(0)
	v_add_f32_e32 v42, v42, v43
	s_nop 1
	v_mov_b32_dpp v43, v42 row_shl:4 row_mask:0xf bank_mask:0x5
	v_mov_b32_dpp v43, v42 row_shr:4 row_mask:0xf bank_mask:0xa
	s_waitcnt lgkmcnt(0)
	v_add_f32_e32 v42, v42, v43
	s_nop 1
	v_mov_b32_dpp v43, v42 quad_perm:[2,3,0,1] row_mask:0xf bank_mask:0xf
	s_waitcnt lgkmcnt(0)
	v_add_f32_e32 v42, v42, v43
	s_nop 1
	v_mov_b32_dpp v43, v42 quad_perm:[1,0,3,2] row_mask:0xf bank_mask:0xf
	s_waitcnt lgkmcnt(0)
	v_add_f32_e32 v42, v42, v43
	v_fmac_f32_e32 v59, 0x3aaaaaab, v42
	v_mul_f32_e32 v42, 0x4f800000, v59
	v_cmp_gt_f32_e32 vcc, s2, v59
	s_waitcnt vmcnt(2)
	v_pk_fma_f32 v[2:3], v[36:37], v[2:3], v[40:41]
	v_cndmask_b32_e32 v42, v59, v42, vcc
	v_sqrt_f32_e32 v43, v42
	v_pk_fma_f32 v[0:1], v[34:35], v[0:1], v[38:39]
	v_add_u32_e32 v44, -1, v43
	v_fma_f32 v45, -v44, v43, v42
	v_cmp_ge_f32_e64 s[0:1], 0, v45
	v_add_u32_e32 v45, 1, v43
	v_cvt_pk_f16_f32 v0, v0, v1
	v_cndmask_b32_e64 v44, v43, v44, s[0:1]
	v_fma_f32 v43, -v45, v43, v42
	v_cmp_lt_f32_e64 s[0:1], 0, v43
	v_cvt_pk_f16_f32 v1, v2, v3
	global_store_dwordx2 v[50:51], v[0:1], off offset:1024
	v_cndmask_b32_e64 v43, v44, v45, s[0:1]
	v_mul_f32_e32 v44, 0x37800000, v43
	v_cndmask_b32_e32 v43, v43, v44, vcc
	v_cmp_class_f32_e32 vcc, v42, v60
	s_nop 1
	v_cndmask_b32_e32 v42, v43, v42, vcc
	v_div_scale_f32 v43, s[0:1], v42, v42, 1.0
	v_rcp_f32_e32 v44, v43
	s_nop 0
	v_fma_f32 v0, -v43, v44, 1.0
	v_fmac_f32_e32 v44, v0, v44
	v_div_scale_f32 v0, vcc, 1.0, v42, 1.0
	v_mul_f32_e32 v1, v0, v44
	v_fma_f32 v2, -v43, v1, v0
	v_fmac_f32_e32 v1, v2, v44
	v_fma_f32 v0, -v43, v1, v0
	v_div_fmas_f32 v0, v0, v44, v1
	v_div_fixup_f32 v0, v0, v42, 1.0
	v_pk_mul_f32 v[4:5], v[4:5], v[0:1] op_sel_hi:[1,0]
	v_pk_mul_f32 v[6:7], v[6:7], v[0:1] op_sel_hi:[1,0]
	v_pk_fma_f32 v[4:5], v[26:27], v[4:5], v[30:31]
	v_pk_fma_f32 v[6:7], v[28:29], v[6:7], v[32:33]
	v_mad_i64_i32 v[2:3], s[0:1], v52, s3, v[24:25]
	v_cvt_pk_f16_f32 v4, v4, v5
	v_cvt_pk_f16_f32 v5, v6, v7
	global_store_dwordx2 v[2:3], v[4:5], off
	v_pk_mul_f32 v[4:5], v[12:13], v[0:1] op_sel_hi:[1,0]
	v_pk_mul_f32 v[6:7], v[14:15], v[0:1] op_sel_hi:[1,0]
	v_pk_fma_f32 v[4:5], v[16:17], v[4:5], v[20:21]
	v_pk_fma_f32 v[6:7], v[18:19], v[6:7], v[22:23]
	v_cvt_pk_f16_f32 v4, v4, v5
	v_cvt_pk_f16_f32 v5, v6, v7
	global_store_dwordx2 v[2:3], v[4:5], off offset:512
	v_pk_mul_f32 v[4:5], v[8:9], v[0:1] op_sel_hi:[1,0]
	v_pk_mul_f32 v[0:1], v[10:11], v[0:1] op_sel_hi:[1,0]
	v_pk_fma_f32 v[4:5], v[34:35], v[4:5], v[38:39]
	v_pk_fma_f32 v[0:1], v[36:37], v[0:1], v[40:41]
	v_cvt_pk_f16_f32 v4, v4, v5
	v_cvt_pk_f16_f32 v5, v0, v1
	global_store_dwordx2 v[2:3], v[4:5], off offset:1024
	s_endpgm
	.p2align	8

	.amdhsa_kernel _Z8prep_ln18PrepArgs
		.amdhsa_group_segment_fixed_size 16640
		.amdhsa_private_segment_fixed_size 0
		.amdhsa_kernarg_size 144
		.amdhsa_user_sgpr_count 2
		.amdhsa_user_sgpr_dispatch_ptr 0
		.amdhsa_user_sgpr_queue_ptr 0
		.amdhsa_user_sgpr_kernarg_segment_ptr 1
		.amdhsa_user_sgpr_dispatch_id 0
		.amdhsa_user_sgpr_kernarg_preload_length 0
		.amdhsa_user_sgpr_kernarg_preload_offset 0
		.amdhsa_user_sgpr_private_segment_size 0
		.amdhsa_uses_dynamic_stack 0
		.amdhsa_enable_private_segment 0
		.amdhsa_system_sgpr_workgroup_id_x 1
		.amdhsa_system_sgpr_workgroup_id_y 0
		.amdhsa_system_sgpr_workgroup_id_z 0
		.amdhsa_system_sgpr_workgroup_info 0
		.amdhsa_system_vgpr_workitem_id 0
		.amdhsa_next_free_vgpr 63
		.amdhsa_next_free_sgpr 16
		.amdhsa_accum_offset 64
		.amdhsa_reserve_vcc 1
		.amdhsa_float_round_mode_32 0
		.amdhsa_float_round_mode_16_64 0
		.amdhsa_float_denorm_mode_32 3
		.amdhsa_float_denorm_mode_16_64 3
		.amdhsa_dx10_clamp 1
		.amdhsa_ieee_mode 1
		.amdhsa_fp16_overflow 0
		.amdhsa_tg_split 0
		.amdhsa_exception_fp_ieee_invalid_op 0
		.amdhsa_exception_fp_denorm_src 0
		.amdhsa_exception_fp_ieee_div_zero 0
		.amdhsa_exception_fp_ieee_overflow 0
		.amdhsa_exception_fp_ieee_underflow 0
		.amdhsa_exception_fp_ieee_inexact 0
		.amdhsa_exception_int_div_zero 0
	.end_amdhsa_kernel

amdhsa.kernels:
  - .agpr_count:     0
    .args:
      - .offset:         0
        .size:           144
        .value_kind:     by_value
    .group_segment_fixed_size: 16640
    .kernarg_segment_align: 8
    .kernarg_segment_size: 144
    .language:       OpenCL C
    .language_version:
      - 2
      - 0
    .max_flat_workgroup_size: 256
    .name:           _Z8prep_ln18PrepArgs
    .private_segment_fixed_size: 0
    .sgpr_count:     22
    .sgpr_spill_count: 0
    .symbol:         _Z8prep_ln18PrepArgs.kd
    .uniform_work_group_size: 1
    .uses_dynamic_stack: false
    .vgpr_count:     63
    .vgpr_spill_count: 0
    .wavefront_size: 64
  - .agpr_count:     0
    .args:
      - .address_space:  global
        .offset:         0
        .size:           8
        .value_kind:     global_buffer
      - .address_space:  global
        .offset:         8
        .size:           8
        .value_kind:     global_buffer
      - .address_space:  global
        .offset:         16
        .size:           8
        .value_kind:     global_buffer
      - .address_space:  global
        .offset:         24
        .size:           8
        .value_kind:     global_buffer
      - .offset:         32
        .size:           144
        .value_kind:     by_value
    .group_segment_fixed_size: 0
    .kernarg_segment_align: 8
    .kernarg_segment_size: 176
    .language:       OpenCL C
    .language_version:
      - 2
      - 0
    .max_flat_workgroup_size: 256
    .name:           _Z10attn64_fwdPKtS0_S0_Pt8PrepArgs
    .private_segment_fixed_size: 0
    .sgpr_count:     42
    .sgpr_spill_count: 0
    .symbol:         _Z10attn64_fwdPKtS0_S0_Pt8PrepArgs.kd
    .uniform_work_group_size: 1
    .uses_dynamic_stack: false
    .vgpr_count:     221
    .vgpr_spill_count: 0
    .wavefront_size: 64
  - .agpr_count:     0
    .args:
      - .address_space:  global
        .offset:         0
        .size:           8
        .value_kind:     global_buffer
      - .address_space:  global
        .offset:         8
        .size:           8
        .value_kind:     global_buffer
      - .offset:         16
        .size:           4
        .value_kind:     by_value
      - .offset:         20
        .size:           4
        .value_kind:     by_value
      - .offset:         24
        .size:           64
        .value_kind:     by_value
    .group_segment_fixed_size: 0
    .kernarg_segment_align: 8
    .kernarg_segment_size: 88
    .language:       OpenCL C
    .language_version:
      - 2
      - 0
    .max_flat_workgroup_size: 256
    .name:           _Z8gemm2b_kILi2EEvPKtS1_ii7EpiArgs
    .private_segment_fixed_size: 0
    .sgpr_count:     98
    .sgpr_spill_count: 0
    .symbol:         _Z8gemm2b_kILi2EEvPKtS1_ii7EpiArgs.kd
    .uniform_work_group_size: 1
    .uses_dynamic_stack: false
    .vgpr_count:     212
    .vgpr_spill_count: 0
    .wavefront_size: 64
  - .agpr_count:     0
    .args:
      - .address_space:  global
        .offset:         0
        .size:           8
        .value_kind:     global_buffer
      - .address_space:  global
        .offset:         8
        .size:           8
        .value_kind:     global_buffer
      - .offset:         16
        .size:           4
        .value_kind:     by_value
      - .offset:         20
        .size:           4
        .value_kind:     by_value
      - .offset:         24
        .size:           64
        .value_kind:     by_value
    .group_segment_fixed_size: 0
    .kernarg_segment_align: 8
    .kernarg_segment_size: 88
    .language:       OpenCL C
    .language_version:
      - 2
      - 0
    .max_flat_workgroup_size: 256
    .name:           _Z8gemm2b_kILi0EEvPKtS1_ii7EpiArgs
    .private_segment_fixed_size: 0
    .sgpr_count:     85
    .sgpr_spill_count: 0
    .symbol:         _Z8gemm2b_kILi0EEvPKtS1_ii7EpiArgs.kd
    .uniform_work_group_size: 1
    .uses_dynamic_stack: false
    .vgpr_count:     186
    .vgpr_spill_count: 0
    .wavefront_size: 64
  - .agpr_count:     0
    .args:
      - .address_space:  global
        .offset:         0
        .size:           8
        .value_kind:     global_buffer
      - .address_space:  global
        .offset:         8
        .size:           8
        .value_kind:     global_buffer
      - .offset:         16
        .size:           4
        .value_kind:     by_value
      - .offset:         20
        .size:           4
        .value_kind:     by_value
      - .offset:         24
        .size:           64
        .value_kind:     by_value
    .group_segment_fixed_size: 0
    .kernarg_segment_align: 8
    .kernarg_segment_size: 88
    .language:       OpenCL C
    .language_version:
      - 2
      - 0
    .max_flat_workgroup_size: 512
    .name:           _Z6gemm_kILi1ELb1ELb0ELb1ELb1ELb0EEvPKtS1_ii7EpiArgs
    .private_segment_fixed_size: 0
    .sgpr_count:     61
    .sgpr_spill_count: 0
    .symbol:         _Z6gemm_kILi1ELb1ELb0ELb1ELb1ELb0EEvPKtS1_ii7EpiArgs.kd
    .uniform_work_group_size: 1
    .uses_dynamic_stack: false
    .vgpr_count:     116
    .vgpr_spill_count: 0
    .wavefront_size: 64
  - .agpr_count:     0
    .args:
      - .address_space:  global
        .offset:         0
        .size:           8
        .value_kind:     global_buffer
      - .address_space:  global
        .offset:         8
        .size:           8
        .value_kind:     global_buffer
      - .offset:         16
        .size:           4
        .value_kind:     by_value
      - .offset:         20
        .size:           4
        .value_kind:     by_value
      - .offset:         24
        .size:           64
        .value_kind:     by_value
    .group_segment_fixed_size: 0
    .kernarg_segment_align: 8
    .kernarg_segment_size: 88
    .language:       OpenCL C
    .language_version:
      - 2
      - 0
    .max_flat_workgroup_size: 512
    .name:           _Z6gemm_kILi1ELb1ELb1ELb0ELb0ELb1EEvPKtS1_ii7EpiArgs
    .private_segment_fixed_size: 0
    .sgpr_count:     84
    .sgpr_spill_count: 0
    .symbol:         _Z6gemm_kILi1ELb1ELb1ELb0ELb0ELb1EEvPKtS1_ii7EpiArgs.kd
    .uniform_work_group_size: 1
    .uses_dynamic_stack: false
    .vgpr_count:     224
    .vgpr_spill_count: 0
    .wavefront_size: 64
